# v27_pad32
# speedup vs baseline: 1.0031x; 1.0005x over previous
.Lp1_lds_1:
	v_mov_b32_e32 v72, v68
	s_nop 0
	ds_read2_b32 v[66:67], v72 offset1:68
	ds_read2_b32 v[68:69], v72 offset0:136 offset1:204
	s_waitcnt lgkmcnt(0)
	s_branch .Lp1_go_1
	s_nop 0
	s_nop 0
	s_nop 0
	s_nop 0
	s_nop 0
	s_nop 0
	s_nop 0
	s_nop 0

.Lp1_lds_2:
	v_mov_b32_e32 v8, v4
	s_nop 0
	ds_read2_b32 v[2:3], v8 offset1:68
	ds_read2_b32 v[4:5], v8 offset0:136 offset1:204
	s_waitcnt lgkmcnt(0)
	s_branch .Lp1_go_2
	s_nop 0
	s_nop 0
	s_nop 0
	s_nop 0
	s_nop 0
	s_nop 0
	s_nop 0
	s_nop 0

.Lp1_lds_4:
	v_mov_b32_e32 v6, v2
	s_nop 0
	ds_read2_b32 v[0:1], v6 offset1:68
	ds_read2_b32 v[2:3], v6 offset0:136 offset1:204
	s_waitcnt lgkmcnt(0)
	s_branch .Lp1_go_4
	s_nop 0
	s_nop 0
	s_nop 0
	s_nop 0
	s_nop 0
	s_nop 0
	s_nop 0
	s_nop 0
